# baseline (speedup 1.0000x reference)
_Z8dog_mainPKfS0_S0_S0_S0_S0_S0_Pf:
	s_load_dwordx8 s[12:19], s[0:1], 0x0
	s_load_dwordx8 s[20:27], s[0:1], 0x20
	s_and_b32 s3, s2, 7
	s_lshl_b32 s3, s3, 5
	s_lshr_b32 s4, s2, 3
	s_add_i32 s4, s3, s4
	s_and_b32 s6, s4, 3
	s_lshr_b32 s7, s4, 2
	s_mov_b32 s5, 0
	s_lshl_b64 s[8:9], s[4:5], 18
	v_and_b32_e32 v1, 63, v0
	v_lshrrev_b32_e32 v2, 6, v0
	v_and_b32_e32 v3, 31, v0
	v_lshl_or_b32 v4, v2, 5, v3
	v_lshlrev_b32_e32 v5, 2, v4
	v_lshlrev_b32_e32 v6, 4, v1
	v_lshl_or_b32 v6, v2, 15, v6
	v_bfe_u32 v7, v0, 5, 1
	s_waitcnt lgkmcnt(0)
	global_load_dword v20, v5, s[18:19]
	global_load_dword v21, v5, s[20:21]
	global_load_dword v22, v5, s[22:23]
	global_load_dword v23, v5, s[24:25]
	global_load_dword v24, v5, s[14:15]
	global_load_dword v25, v5, s[16:17]
	s_lshl_b32 s10, s6, 6
	s_add_i32 s10, s10, s7
	s_lshl_b32 s10, s10, 10
	v_add_u32_e32 v31, s10, v5
	global_load_dword v26, v31, s[26:27]
	s_add_u32 s12, s12, s8
	s_addc_u32 s13, s13, s9
	v_lshlrev_b32_e32 v6, 4, v1
	v_bfe_u32 v16, v2, 0, 1
	v_lshl_or_b32 v6, v16, 12, v6
	v_bfe_u32 v16, v2, 1, 1
	v_lshl_or_b32 v6, v16, 13, v6
	v_bfe_u32 v16, v2, 2, 1
	v_lshl_or_b32 v6, v16, 14, v6
	global_load_dwordx4 v[128:131], v6, s[12:13] nt
	global_load_dwordx4 v[132:135], v6, s[12:13] offset:1024 nt
	global_load_dwordx4 v[136:139], v6, s[12:13] offset:2048 nt
	global_load_dwordx4 v[140:143], v6, s[12:13] offset:3072 nt
	v_add_u32_e32 v17, 0x8000, v6
	global_load_dwordx4 v[144:147], v17, s[12:13] nt
	v_add_u32_e32 v17, 0x8400, v6
	global_load_dwordx4 v[148:151], v17, s[12:13] nt
	v_add_u32_e32 v17, 0x8800, v6
	global_load_dwordx4 v[152:155], v17, s[12:13] nt
	v_add_u32_e32 v17, 0x8c00, v6
	global_load_dwordx4 v[156:159], v17, s[12:13] nt
	v_add_u32_e32 v17, 0x10000, v6
	global_load_dwordx4 v[160:163], v17, s[12:13] nt
	v_add_u32_e32 v17, 0x10400, v6
	global_load_dwordx4 v[164:167], v17, s[12:13] nt
	v_add_u32_e32 v17, 0x10800, v6
	global_load_dwordx4 v[168:171], v17, s[12:13] nt
	v_add_u32_e32 v17, 0x10c00, v6
	global_load_dwordx4 v[172:175], v17, s[12:13] nt
	v_add_u32_e32 v17, 0x18000, v6
	global_load_dwordx4 v[176:179], v17, s[12:13] nt
	v_add_u32_e32 v17, 0x18400, v6
	global_load_dwordx4 v[180:183], v17, s[12:13] nt
	v_add_u32_e32 v17, 0x18800, v6
	global_load_dwordx4 v[184:187], v17, s[12:13] nt
	v_add_u32_e32 v17, 0x18c00, v6
	global_load_dwordx4 v[188:191], v17, s[12:13] nt
	v_add_u32_e32 v17, 0x20000, v6
	global_load_dwordx4 v[192:195], v17, s[12:13] nt
	v_add_u32_e32 v17, 0x20400, v6
	global_load_dwordx4 v[196:199], v17, s[12:13] nt
	v_add_u32_e32 v17, 0x20800, v6
	global_load_dwordx4 v[200:203], v17, s[12:13] nt
	v_add_u32_e32 v17, 0x20c00, v6
	global_load_dwordx4 v[204:207], v17, s[12:13] nt
	v_add_u32_e32 v17, 0x28000, v6
	global_load_dwordx4 v[208:211], v17, s[12:13] nt
	v_add_u32_e32 v17, 0x28400, v6
	global_load_dwordx4 v[212:215], v17, s[12:13] nt
	v_add_u32_e32 v17, 0x28800, v6
	global_load_dwordx4 v[216:219], v17, s[12:13] nt
	v_add_u32_e32 v17, 0x28c00, v6
	global_load_dwordx4 v[220:223], v17, s[12:13] nt
	v_add_u32_e32 v17, 0x30000, v6
	global_load_dwordx4 v[224:227], v17, s[12:13] nt
	v_add_u32_e32 v17, 0x30400, v6
	global_load_dwordx4 v[228:231], v17, s[12:13] nt
	v_add_u32_e32 v17, 0x30800, v6
	global_load_dwordx4 v[232:235], v17, s[12:13] nt
	v_add_u32_e32 v17, 0x30c00, v6
	global_load_dwordx4 v[236:239], v17, s[12:13] nt
	v_add_u32_e32 v17, 0x38000, v6
	global_load_dwordx4 v[240:243], v17, s[12:13] nt
	v_add_u32_e32 v17, 0x38400, v6
	global_load_dwordx4 v[244:247], v17, s[12:13] nt
	v_add_u32_e32 v17, 0x38800, v6
	global_load_dwordx4 v[248:251], v17, s[12:13] nt
	v_add_u32_e32 v17, 0x38c00, v6
	global_load_dwordx4 v[252:255], v17, s[12:13] nt
	v_and_b32_e32 v16, 1, v0
	v_cmp_eq_u32_e64 s[30:31], 0, v16
	v_and_b32_e32 v17, 2, v0
	v_cmp_eq_u32_e64 s[32:33], 0, v17
	v_lshrrev_b32_e32 v17, 2, v1
	v_lshlrev_b32_e32 v14, 1, v17
	v_bfe_u32 v16, v2, 0, 1
	s_movk_i32 s10, 0x80
	v_mad_u32_u24 v14, v16, s10, v14
	v_bfe_u32 v16, v2, 1, 1
	s_movk_i32 s10, 0x110
	v_mad_u32_u24 v14, v16, s10, v14
	v_bfe_u32 v16, v2, 2, 1
	s_movk_i32 s10, 0x220
	v_mad_u32_u24 v14, v16, s10, v14
	v_bfe_u32 v16, v0, 0, 1
	s_movk_i32 s10, 0x20
	v_mad_u32_u24 v14, v16, s10, v14
	v_bfe_u32 v16, v0, 1, 1
	s_movk_i32 s10, 0x40
	v_mad_u32_u24 v14, v16, s10, v14
	s_movk_i32 s10, 0x110
	v_lshlrev_b32_e32 v17, 4, v7
	v_mad_u32_u24 v15, v3, s10, v17
	s_lshl_b32 s11, s6, 5
	v_lshl_add_u32 v18, v7, 2, s11
	v_cvt_f32_u32_e32 v18, v18
	v_lshlrev_b32_e32 v19, 3, v7
	v_cvt_f32_u32_e32 v19, v19
	s_waitcnt vmcnt(32)
	v_add_f32_e32 v26, v20, v21
	v_rcp_f32_e32 v27, v20
	v_rcp_f32_e32 v28, v26
	v_sub_f32_e32 v12, v19, v22
	v_sub_f32_e32 v13, v18, v23
	v_fma_f32 v29, -v20, v27, 1.0
	v_fma_f32 v30, -v26, v28, 1.0
	v_fma_f32 v27, v29, v27, v27
	v_fma_f32 v28, v30, v28, v28
	v_mul_f32_e32 v8, 0xbf38aa3b, v27
	v_mul_f32_e32 v9, 0xbf38aa3b, v28
	v_mul_f32_e32 v29, v24, v27
	v_mul_f32_e32 v30, v25, v28
	v_mul_f32_e32 v10, 0x3e22f983, v29
	v_mul_f32_e32 v11, 0x3e22f983, v30
	v_mul_f32_e32 v16, v12, v12
	v_add_f32_e32 v17, 0x3f800000, v12
	v_add_f32_e32 v18, 0x40000000, v12
	v_add_f32_e32 v19, 0x40400000, v12
	v_mul_f32_e32 v17, v17, v17
	v_mul_f32_e32 v18, v18, v18
	v_mul_f32_e32 v19, v19, v19
	v_mul_f32_e32 v20, v8, v16
	v_mul_f32_e32 v24, v9, v16
	v_mul_f32_e32 v21, v8, v17
	v_mul_f32_e32 v25, v9, v17
	v_mul_f32_e32 v22, v8, v18
	v_mul_f32_e32 v26, v9, v18
	v_mul_f32_e32 v23, v8, v19
	v_mul_f32_e32 v27, v9, v19
	v_exp_f32_e32 v20, v20
	v_exp_f32_e32 v21, v21
	v_exp_f32_e32 v22, v22
	v_exp_f32_e32 v23, v23
	v_exp_f32_e32 v24, v24
	v_exp_f32_e32 v25, v25
	v_exp_f32_e32 v26, v26
	v_exp_f32_e32 v27, v27
	v_cvt_pk_f16_f32 v32, v20, v21
	v_cvt_pk_f16_f32 v33, v22, v23
	v_cvt_pk_f16_f32 v64, v24, v25
	v_cvt_pk_f16_f32 v65, v26, v27
	v_add_f32_e32 v16, 0x40800000, v12
	v_add_f32_e32 v17, 0x40a00000, v12
	v_add_f32_e32 v18, 0x40c00000, v12
	v_add_f32_e32 v19, 0x40e00000, v12
	v_mul_f32_e32 v16, v16, v16
	v_mul_f32_e32 v17, v17, v17
	v_mul_f32_e32 v18, v18, v18
	v_mul_f32_e32 v19, v19, v19
	v_mul_f32_e32 v20, v8, v16
	v_mul_f32_e32 v24, v9, v16
	v_mul_f32_e32 v21, v8, v17
	v_mul_f32_e32 v25, v9, v17
	v_mul_f32_e32 v22, v8, v18
	v_mul_f32_e32 v26, v9, v18
	v_mul_f32_e32 v23, v8, v19
	v_mul_f32_e32 v27, v9, v19
	v_exp_f32_e32 v20, v20
	v_exp_f32_e32 v21, v21
	v_exp_f32_e32 v22, v22
	v_exp_f32_e32 v23, v23
	v_exp_f32_e32 v24, v24
	v_exp_f32_e32 v25, v25
	v_exp_f32_e32 v26, v26
	v_exp_f32_e32 v27, v27
	v_cvt_pk_f16_f32 v34, v20, v21
	v_cvt_pk_f16_f32 v35, v22, v23
	v_cvt_pk_f16_f32 v66, v24, v25
	v_cvt_pk_f16_f32 v67, v26, v27
	v_add_f32_e32 v16, 0x41800000, v12
	v_add_f32_e32 v17, 0x41880000, v12
	v_add_f32_e32 v18, 0x41900000, v12
	v_add_f32_e32 v19, 0x41980000, v12
	v_mul_f32_e32 v16, v16, v16
	v_mul_f32_e32 v17, v17, v17
	v_mul_f32_e32 v18, v18, v18
	v_mul_f32_e32 v19, v19, v19
	v_mul_f32_e32 v20, v8, v16
	v_mul_f32_e32 v24, v9, v16
	v_mul_f32_e32 v21, v8, v17
	v_mul_f32_e32 v25, v9, v17
	v_mul_f32_e32 v22, v8, v18
	v_mul_f32_e32 v26, v9, v18
	v_mul_f32_e32 v23, v8, v19
	v_mul_f32_e32 v27, v9, v19
	v_exp_f32_e32 v20, v20
	v_exp_f32_e32 v21, v21
	v_exp_f32_e32 v22, v22
	v_exp_f32_e32 v23, v23
	v_exp_f32_e32 v24, v24
	v_exp_f32_e32 v25, v25
	v_exp_f32_e32 v26, v26
	v_exp_f32_e32 v27, v27
	v_cvt_pk_f16_f32 v36, v20, v21
	v_cvt_pk_f16_f32 v37, v22, v23
	v_cvt_pk_f16_f32 v68, v24, v25
	v_cvt_pk_f16_f32 v69, v26, v27
	v_add_f32_e32 v16, 0x41a00000, v12
	v_add_f32_e32 v17, 0x41a80000, v12
	v_add_f32_e32 v18, 0x41b00000, v12
	v_add_f32_e32 v19, 0x41b80000, v12
	v_mul_f32_e32 v16, v16, v16
	v_mul_f32_e32 v17, v17, v17
	v_mul_f32_e32 v18, v18, v18
	v_mul_f32_e32 v19, v19, v19
	v_mul_f32_e32 v20, v8, v16
	v_mul_f32_e32 v24, v9, v16
	v_mul_f32_e32 v21, v8, v17
	v_mul_f32_e32 v25, v9, v17
	v_mul_f32_e32 v22, v8, v18
	v_mul_f32_e32 v26, v9, v18
	v_mul_f32_e32 v23, v8, v19
	v_mul_f32_e32 v27, v9, v19
	v_exp_f32_e32 v20, v20
	v_exp_f32_e32 v21, v21
	v_exp_f32_e32 v22, v22
	v_exp_f32_e32 v23, v23
	v_exp_f32_e32 v24, v24
	v_exp_f32_e32 v25, v25
	v_exp_f32_e32 v26, v26
	v_exp_f32_e32 v27, v27
	v_cvt_pk_f16_f32 v38, v20, v21
	v_cvt_pk_f16_f32 v39, v22, v23
	v_cvt_pk_f16_f32 v70, v24, v25
	v_cvt_pk_f16_f32 v71, v26, v27
	v_add_f32_e32 v16, 0x42000000, v12
	v_add_f32_e32 v17, 0x42040000, v12
	v_add_f32_e32 v18, 0x42080000, v12
	v_add_f32_e32 v19, 0x420c0000, v12
	v_mul_f32_e32 v16, v16, v16
	v_mul_f32_e32 v17, v17, v17
	v_mul_f32_e32 v18, v18, v18
	v_mul_f32_e32 v19, v19, v19
	v_mul_f32_e32 v20, v8, v16
	v_mul_f32_e32 v24, v9, v16
	v_mul_f32_e32 v21, v8, v17
	v_mul_f32_e32 v25, v9, v17
	v_mul_f32_e32 v22, v8, v18
	v_mul_f32_e32 v26, v9, v18
	v_mul_f32_e32 v23, v8, v19
	v_mul_f32_e32 v27, v9, v19
	v_exp_f32_e32 v20, v20
	v_exp_f32_e32 v21, v21
	v_exp_f32_e32 v22, v22
	v_exp_f32_e32 v23, v23
	v_exp_f32_e32 v24, v24
	v_exp_f32_e32 v25, v25
	v_exp_f32_e32 v26, v26
	v_exp_f32_e32 v27, v27
	v_cvt_pk_f16_f32 v40, v20, v21
	v_cvt_pk_f16_f32 v41, v22, v23
	v_cvt_pk_f16_f32 v72, v24, v25
	v_cvt_pk_f16_f32 v73, v26, v27
	v_add_f32_e32 v16, 0x42100000, v12
	v_add_f32_e32 v17, 0x42140000, v12
	v_add_f32_e32 v18, 0x42180000, v12
	v_add_f32_e32 v19, 0x421c0000, v12
	v_mul_f32_e32 v16, v16, v16
	v_mul_f32_e32 v17, v17, v17
	v_mul_f32_e32 v18, v18, v18
	v_mul_f32_e32 v19, v19, v19
	v_mul_f32_e32 v20, v8, v16
	v_mul_f32_e32 v24, v9, v16
	v_mul_f32_e32 v21, v8, v17
	v_mul_f32_e32 v25, v9, v17
	v_mul_f32_e32 v22, v8, v18
	v_mul_f32_e32 v26, v9, v18
	v_mul_f32_e32 v23, v8, v19
	v_mul_f32_e32 v27, v9, v19
	v_exp_f32_e32 v20, v20
	v_exp_f32_e32 v21, v21
	v_exp_f32_e32 v22, v22
	v_exp_f32_e32 v23, v23
	v_exp_f32_e32 v24, v24
	v_exp_f32_e32 v25, v25
	v_exp_f32_e32 v26, v26
	v_exp_f32_e32 v27, v27
	v_cvt_pk_f16_f32 v42, v20, v21
	v_cvt_pk_f16_f32 v43, v22, v23
	v_cvt_pk_f16_f32 v74, v24, v25
	v_cvt_pk_f16_f32 v75, v26, v27
	v_add_f32_e32 v16, 0x42400000, v12
	v_add_f32_e32 v17, 0x42440000, v12
	v_add_f32_e32 v18, 0x42480000, v12
	v_add_f32_e32 v19, 0x424c0000, v12
	v_mul_f32_e32 v16, v16, v16
	v_mul_f32_e32 v17, v17, v17
	v_mul_f32_e32 v18, v18, v18
	v_mul_f32_e32 v19, v19, v19
	v_mul_f32_e32 v20, v8, v16
	v_mul_f32_e32 v24, v9, v16
	v_mul_f32_e32 v21, v8, v17
	v_mul_f32_e32 v25, v9, v17
	v_mul_f32_e32 v22, v8, v18
	v_mul_f32_e32 v26, v9, v18
	v_mul_f32_e32 v23, v8, v19
	v_mul_f32_e32 v27, v9, v19
	v_exp_f32_e32 v20, v20
	v_exp_f32_e32 v21, v21
	v_exp_f32_e32 v22, v22
	v_exp_f32_e32 v23, v23
	v_exp_f32_e32 v24, v24
	v_exp_f32_e32 v25, v25
	v_exp_f32_e32 v26, v26
	v_exp_f32_e32 v27, v27
	v_cvt_pk_f16_f32 v44, v20, v21
	v_cvt_pk_f16_f32 v45, v22, v23
	v_cvt_pk_f16_f32 v76, v24, v25
	v_cvt_pk_f16_f32 v77, v26, v27
	v_add_f32_e32 v16, 0x42500000, v12
	v_add_f32_e32 v17, 0x42540000, v12
	v_add_f32_e32 v18, 0x42580000, v12
	v_add_f32_e32 v19, 0x425c0000, v12
	v_mul_f32_e32 v16, v16, v16
	v_mul_f32_e32 v17, v17, v17
	v_mul_f32_e32 v18, v18, v18
	v_mul_f32_e32 v19, v19, v19
	v_mul_f32_e32 v20, v8, v16
	v_mul_f32_e32 v24, v9, v16
	v_mul_f32_e32 v21, v8, v17
	v_mul_f32_e32 v25, v9, v17
	v_mul_f32_e32 v22, v8, v18
	v_mul_f32_e32 v26, v9, v18
	v_mul_f32_e32 v23, v8, v19
	v_mul_f32_e32 v27, v9, v19
	v_exp_f32_e32 v20, v20
	v_exp_f32_e32 v21, v21
	v_exp_f32_e32 v22, v22
	v_exp_f32_e32 v23, v23
	v_exp_f32_e32 v24, v24
	v_exp_f32_e32 v25, v25
	v_exp_f32_e32 v26, v26
	v_exp_f32_e32 v27, v27
	v_cvt_pk_f16_f32 v46, v20, v21
	v_cvt_pk_f16_f32 v47, v22, v23
	v_cvt_pk_f16_f32 v78, v24, v25
	v_cvt_pk_f16_f32 v79, v26, v27
	v_add_f32_e32 v16, 0x42800000, v12
	v_add_f32_e32 v17, 0x42820000, v12
	v_add_f32_e32 v18, 0x42840000, v12
	v_add_f32_e32 v19, 0x42860000, v12
	v_mul_f32_e32 v16, v16, v16
	v_mul_f32_e32 v17, v17, v17
	v_mul_f32_e32 v18, v18, v18
	v_mul_f32_e32 v19, v19, v19
	v_mul_f32_e32 v20, v8, v16
	v_mul_f32_e32 v24, v9, v16
	v_mul_f32_e32 v21, v8, v17
	v_mul_f32_e32 v25, v9, v17
	v_mul_f32_e32 v22, v8, v18
	v_mul_f32_e32 v26, v9, v18
	v_mul_f32_e32 v23, v8, v19
	v_mul_f32_e32 v27, v9, v19
	v_exp_f32_e32 v20, v20
	v_exp_f32_e32 v21, v21
	v_exp_f32_e32 v22, v22
	v_exp_f32_e32 v23, v23
	v_exp_f32_e32 v24, v24
	v_exp_f32_e32 v25, v25
	v_exp_f32_e32 v26, v26
	v_exp_f32_e32 v27, v27
	v_cvt_pk_f16_f32 v48, v20, v21
	v_cvt_pk_f16_f32 v49, v22, v23
	v_cvt_pk_f16_f32 v80, v24, v25
	v_cvt_pk_f16_f32 v81, v26, v27
	v_add_f32_e32 v16, 0x42880000, v12
	v_add_f32_e32 v17, 0x428a0000, v12
	v_add_f32_e32 v18, 0x428c0000, v12
	v_add_f32_e32 v19, 0x428e0000, v12
	v_mul_f32_e32 v16, v16, v16
	v_mul_f32_e32 v17, v17, v17
	v_mul_f32_e32 v18, v18, v18
	v_mul_f32_e32 v19, v19, v19
	v_mul_f32_e32 v20, v8, v16
	v_mul_f32_e32 v24, v9, v16
	v_mul_f32_e32 v21, v8, v17
	v_mul_f32_e32 v25, v9, v17
	v_mul_f32_e32 v22, v8, v18
	v_mul_f32_e32 v26, v9, v18
	v_mul_f32_e32 v23, v8, v19
	v_mul_f32_e32 v27, v9, v19
	v_exp_f32_e32 v20, v20
	v_exp_f32_e32 v21, v21
	v_exp_f32_e32 v22, v22
	v_exp_f32_e32 v23, v23
	v_exp_f32_e32 v24, v24
	v_exp_f32_e32 v25, v25
	v_exp_f32_e32 v26, v26
	v_exp_f32_e32 v27, v27
	v_cvt_pk_f16_f32 v50, v20, v21
	v_cvt_pk_f16_f32 v51, v22, v23
	v_cvt_pk_f16_f32 v82, v24, v25
	v_cvt_pk_f16_f32 v83, v26, v27
	v_add_f32_e32 v16, 0x42a00000, v12
	v_add_f32_e32 v17, 0x42a20000, v12
	v_add_f32_e32 v18, 0x42a40000, v12
	v_add_f32_e32 v19, 0x42a60000, v12
	v_mul_f32_e32 v16, v16, v16
	v_mul_f32_e32 v17, v17, v17
	v_mul_f32_e32 v18, v18, v18
	v_mul_f32_e32 v19, v19, v19
	v_mul_f32_e32 v20, v8, v16
	v_mul_f32_e32 v24, v9, v16
	v_mul_f32_e32 v21, v8, v17
	v_mul_f32_e32 v25, v9, v17
	v_mul_f32_e32 v22, v8, v18
	v_mul_f32_e32 v26, v9, v18
	v_mul_f32_e32 v23, v8, v19
	v_mul_f32_e32 v27, v9, v19
	v_exp_f32_e32 v20, v20
	v_exp_f32_e32 v21, v21
	v_exp_f32_e32 v22, v22
	v_exp_f32_e32 v23, v23
	v_exp_f32_e32 v24, v24
	v_exp_f32_e32 v25, v25
	v_exp_f32_e32 v26, v26
	v_exp_f32_e32 v27, v27
	v_cvt_pk_f16_f32 v52, v20, v21
	v_cvt_pk_f16_f32 v53, v22, v23
	v_cvt_pk_f16_f32 v84, v24, v25
	v_cvt_pk_f16_f32 v85, v26, v27
	v_add_f32_e32 v16, 0x42a80000, v12
	v_add_f32_e32 v17, 0x42aa0000, v12
	v_add_f32_e32 v18, 0x42ac0000, v12
	v_add_f32_e32 v19, 0x42ae0000, v12
	v_mul_f32_e32 v16, v16, v16
	v_mul_f32_e32 v17, v17, v17
	v_mul_f32_e32 v18, v18, v18
	v_mul_f32_e32 v19, v19, v19
	v_mul_f32_e32 v20, v8, v16
	v_mul_f32_e32 v24, v9, v16
	v_mul_f32_e32 v21, v8, v17
	v_mul_f32_e32 v25, v9, v17
	v_mul_f32_e32 v22, v8, v18
	v_mul_f32_e32 v26, v9, v18
	v_mul_f32_e32 v23, v8, v19
	v_mul_f32_e32 v27, v9, v19
	v_exp_f32_e32 v20, v20
	v_exp_f32_e32 v21, v21
	v_exp_f32_e32 v22, v22
	v_exp_f32_e32 v23, v23
	v_exp_f32_e32 v24, v24
	v_exp_f32_e32 v25, v25
	v_exp_f32_e32 v26, v26
	v_exp_f32_e32 v27, v27
	v_cvt_pk_f16_f32 v54, v20, v21
	v_cvt_pk_f16_f32 v55, v22, v23
	v_cvt_pk_f16_f32 v86, v24, v25
	v_cvt_pk_f16_f32 v87, v26, v27
	v_add_f32_e32 v16, 0x42c00000, v12
	v_add_f32_e32 v17, 0x42c20000, v12
	v_add_f32_e32 v18, 0x42c40000, v12
	v_add_f32_e32 v19, 0x42c60000, v12
	v_mul_f32_e32 v16, v16, v16
	v_mul_f32_e32 v17, v17, v17
	v_mul_f32_e32 v18, v18, v18
	v_mul_f32_e32 v19, v19, v19
	v_mul_f32_e32 v20, v8, v16
	v_mul_f32_e32 v24, v9, v16
	v_mul_f32_e32 v21, v8, v17
	v_mul_f32_e32 v25, v9, v17
	v_mul_f32_e32 v22, v8, v18
	v_mul_f32_e32 v26, v9, v18
	v_mul_f32_e32 v23, v8, v19
	v_mul_f32_e32 v27, v9, v19
	v_exp_f32_e32 v20, v20
	v_exp_f32_e32 v21, v21
	v_exp_f32_e32 v22, v22
	v_exp_f32_e32 v23, v23
	v_exp_f32_e32 v24, v24
	v_exp_f32_e32 v25, v25
	v_exp_f32_e32 v26, v26
	v_exp_f32_e32 v27, v27
	v_cvt_pk_f16_f32 v56, v20, v21
	v_cvt_pk_f16_f32 v57, v22, v23
	v_cvt_pk_f16_f32 v88, v24, v25
	v_cvt_pk_f16_f32 v89, v26, v27
	v_add_f32_e32 v16, 0x42c80000, v12
	v_add_f32_e32 v17, 0x42ca0000, v12
	v_add_f32_e32 v18, 0x42cc0000, v12
	v_add_f32_e32 v19, 0x42ce0000, v12
	v_mul_f32_e32 v16, v16, v16
	v_mul_f32_e32 v17, v17, v17
	v_mul_f32_e32 v18, v18, v18
	v_mul_f32_e32 v19, v19, v19
	v_mul_f32_e32 v20, v8, v16
	v_mul_f32_e32 v24, v9, v16
	v_mul_f32_e32 v21, v8, v17
	v_mul_f32_e32 v25, v9, v17
	v_mul_f32_e32 v22, v8, v18
	v_mul_f32_e32 v26, v9, v18
	v_mul_f32_e32 v23, v8, v19
	v_mul_f32_e32 v27, v9, v19
	v_exp_f32_e32 v20, v20
	v_exp_f32_e32 v21, v21
	v_exp_f32_e32 v22, v22
	v_exp_f32_e32 v23, v23
	v_exp_f32_e32 v24, v24
	v_exp_f32_e32 v25, v25
	v_exp_f32_e32 v26, v26
	v_exp_f32_e32 v27, v27
	v_cvt_pk_f16_f32 v58, v20, v21
	v_cvt_pk_f16_f32 v59, v22, v23
	v_cvt_pk_f16_f32 v90, v24, v25
	v_cvt_pk_f16_f32 v91, v26, v27
	v_add_f32_e32 v16, 0x42e00000, v12
	v_add_f32_e32 v17, 0x42e20000, v12
	v_add_f32_e32 v18, 0x42e40000, v12
	v_add_f32_e32 v19, 0x42e60000, v12
	v_mul_f32_e32 v16, v16, v16
	v_mul_f32_e32 v17, v17, v17
	v_mul_f32_e32 v18, v18, v18
	v_mul_f32_e32 v19, v19, v19
	v_mul_f32_e32 v20, v8, v16
	v_mul_f32_e32 v24, v9, v16
	v_mul_f32_e32 v21, v8, v17
	v_mul_f32_e32 v25, v9, v17
	v_mul_f32_e32 v22, v8, v18
	v_mul_f32_e32 v26, v9, v18
	v_mul_f32_e32 v23, v8, v19
	v_mul_f32_e32 v27, v9, v19
	v_exp_f32_e32 v20, v20
	v_exp_f32_e32 v21, v21
	v_exp_f32_e32 v22, v22
	v_exp_f32_e32 v23, v23
	v_exp_f32_e32 v24, v24
	v_exp_f32_e32 v25, v25
	v_exp_f32_e32 v26, v26
	v_exp_f32_e32 v27, v27
	v_cvt_pk_f16_f32 v60, v20, v21
	v_cvt_pk_f16_f32 v61, v22, v23
	v_cvt_pk_f16_f32 v92, v24, v25
	v_cvt_pk_f16_f32 v93, v26, v27
	v_add_f32_e32 v16, 0x42e80000, v12
	v_add_f32_e32 v17, 0x42ea0000, v12
	v_add_f32_e32 v18, 0x42ec0000, v12
	v_add_f32_e32 v19, 0x42ee0000, v12
	v_mul_f32_e32 v16, v16, v16
	v_mul_f32_e32 v17, v17, v17
	v_mul_f32_e32 v18, v18, v18
	v_mul_f32_e32 v19, v19, v19
	v_mul_f32_e32 v20, v8, v16
	v_mul_f32_e32 v24, v9, v16
	v_mul_f32_e32 v21, v8, v17
	v_mul_f32_e32 v25, v9, v17
	v_mul_f32_e32 v22, v8, v18
	v_mul_f32_e32 v26, v9, v18
	v_mul_f32_e32 v23, v8, v19
	v_mul_f32_e32 v27, v9, v19
	v_exp_f32_e32 v20, v20
	v_exp_f32_e32 v21, v21
	v_exp_f32_e32 v22, v22
	v_exp_f32_e32 v23, v23
	v_exp_f32_e32 v24, v24
	v_exp_f32_e32 v25, v25
	v_exp_f32_e32 v26, v26
	v_exp_f32_e32 v27, v27
	v_cvt_pk_f16_f32 v62, v20, v21
	v_cvt_pk_f16_f32 v63, v22, v23
	v_cvt_pk_f16_f32 v94, v24, v25
	v_cvt_pk_f16_f32 v95, v26, v27
	v_mul_f32_e32 v16, v13, v13
	v_add_f32_e32 v17, 0x3f800000, v13
	v_add_f32_e32 v18, 0x40000000, v13
	v_add_f32_e32 v19, 0x40400000, v13
	v_mul_f32_e32 v17, v17, v17
	v_mul_f32_e32 v18, v18, v18
	v_mul_f32_e32 v19, v19, v19
	v_mul_f32_e32 v20, v8, v16
	v_mul_f32_e32 v24, v9, v16
	v_mul_f32_e32 v21, v8, v17
	v_mul_f32_e32 v25, v9, v17
	v_mul_f32_e32 v22, v8, v18
	v_mul_f32_e32 v26, v9, v18
	v_mul_f32_e32 v23, v8, v19
	v_mul_f32_e32 v27, v9, v19
	v_exp_f32_e32 v20, v20
	v_exp_f32_e32 v21, v21
	v_exp_f32_e32 v22, v22
	v_exp_f32_e32 v23, v23
	v_exp_f32_e32 v24, v24
	v_exp_f32_e32 v25, v25
	v_exp_f32_e32 v26, v26
	v_exp_f32_e32 v27, v27
	v_mul_f32_e32 v96, v10, v20
	v_mul_f32_e32 v97, v10, v21
	v_mul_f32_e32 v98, v10, v22
	v_mul_f32_e32 v99, v10, v23
	v_mul_f32_e32 v112, v11, v24
	v_mul_f32_e32 v113, v11, v25
	v_mul_f32_e32 v114, v11, v26
	v_mul_f32_e32 v115, v11, v27
	v_add_f32_e32 v16, 0x41000000, v13
	v_add_f32_e32 v17, 0x41100000, v13
	v_add_f32_e32 v18, 0x41200000, v13
	v_add_f32_e32 v19, 0x41300000, v13
	v_mul_f32_e32 v16, v16, v16
	v_mul_f32_e32 v17, v17, v17
	v_mul_f32_e32 v18, v18, v18
	v_mul_f32_e32 v19, v19, v19
	v_mul_f32_e32 v20, v8, v16
	v_mul_f32_e32 v24, v9, v16
	v_mul_f32_e32 v21, v8, v17
	v_mul_f32_e32 v25, v9, v17
	v_mul_f32_e32 v22, v8, v18
	v_mul_f32_e32 v26, v9, v18
	v_mul_f32_e32 v23, v8, v19
	v_mul_f32_e32 v27, v9, v19
	v_exp_f32_e32 v20, v20
	v_exp_f32_e32 v21, v21
	v_exp_f32_e32 v22, v22
	v_exp_f32_e32 v23, v23
	v_exp_f32_e32 v24, v24
	v_exp_f32_e32 v25, v25
	v_exp_f32_e32 v26, v26
	v_exp_f32_e32 v27, v27
	v_mul_f32_e32 v100, v10, v20
	v_mul_f32_e32 v101, v10, v21
	v_mul_f32_e32 v102, v10, v22
	v_mul_f32_e32 v103, v10, v23
	v_mul_f32_e32 v116, v11, v24
	v_mul_f32_e32 v117, v11, v25
	v_mul_f32_e32 v118, v11, v26
	v_mul_f32_e32 v119, v11, v27
	v_add_f32_e32 v16, 0x41800000, v13
	v_add_f32_e32 v17, 0x41880000, v13
	v_add_f32_e32 v18, 0x41900000, v13
	v_add_f32_e32 v19, 0x41980000, v13
	v_mul_f32_e32 v16, v16, v16
	v_mul_f32_e32 v17, v17, v17
	v_mul_f32_e32 v18, v18, v18
	v_mul_f32_e32 v19, v19, v19
	v_mul_f32_e32 v20, v8, v16
	v_mul_f32_e32 v24, v9, v16
	v_mul_f32_e32 v21, v8, v17
	v_mul_f32_e32 v25, v9, v17
	v_mul_f32_e32 v22, v8, v18
	v_mul_f32_e32 v26, v9, v18
	v_mul_f32_e32 v23, v8, v19
	v_mul_f32_e32 v27, v9, v19
	v_exp_f32_e32 v20, v20
	v_exp_f32_e32 v21, v21
	v_exp_f32_e32 v22, v22
	v_exp_f32_e32 v23, v23
	v_exp_f32_e32 v24, v24
	v_exp_f32_e32 v25, v25
	v_exp_f32_e32 v26, v26
	v_exp_f32_e32 v27, v27
	v_mul_f32_e32 v104, v10, v20
	v_mul_f32_e32 v105, v10, v21
	v_mul_f32_e32 v106, v10, v22
	v_mul_f32_e32 v107, v10, v23
	v_mul_f32_e32 v120, v11, v24
	v_mul_f32_e32 v121, v11, v25
	v_mul_f32_e32 v122, v11, v26
	v_mul_f32_e32 v123, v11, v27
	v_add_f32_e32 v16, 0x41c00000, v13
	v_add_f32_e32 v17, 0x41c80000, v13
	v_add_f32_e32 v18, 0x41d00000, v13
	v_add_f32_e32 v19, 0x41d80000, v13
	v_mul_f32_e32 v16, v16, v16
	v_mul_f32_e32 v17, v17, v17
	v_mul_f32_e32 v18, v18, v18
	v_mul_f32_e32 v19, v19, v19
	v_mul_f32_e32 v20, v8, v16
	v_mul_f32_e32 v24, v9, v16
	v_mul_f32_e32 v21, v8, v17
	v_mul_f32_e32 v25, v9, v17
	v_mul_f32_e32 v22, v8, v18
	v_mul_f32_e32 v26, v9, v18
	v_mul_f32_e32 v23, v8, v19
	v_mul_f32_e32 v27, v9, v19
	v_exp_f32_e32 v20, v20
	v_exp_f32_e32 v21, v21
	v_exp_f32_e32 v22, v22
	v_exp_f32_e32 v23, v23
	v_exp_f32_e32 v24, v24
	v_exp_f32_e32 v25, v25
	v_exp_f32_e32 v26, v26
	v_exp_f32_e32 v27, v27
	v_mul_f32_e32 v108, v10, v20
	v_mul_f32_e32 v109, v10, v21
	v_mul_f32_e32 v110, v10, v22
	v_mul_f32_e32 v111, v10, v23
	v_mul_f32_e32 v124, v11, v24
	v_mul_f32_e32 v125, v11, v25
	v_mul_f32_e32 v126, v11, v26
	v_mul_f32_e32 v127, v11, v27
	s_waitcnt vmcnt(28)
	v_add_f32_e32 v128, v128, v129
	v_add_f32_e32 v130, v130, v131
	v_add_f32_e32 v132, v132, v133
	v_add_f32_e32 v134, v134, v135
	v_add_f32_e32 v136, v136, v137
	v_add_f32_e32 v138, v138, v139
	v_add_f32_e32 v140, v140, v141
	v_add_f32_e32 v142, v142, v143
	v_add_f32_e32 v128, v128, v130
	v_add_f32_e32 v132, v132, v134
	v_add_f32_e32 v136, v136, v138
	v_add_f32_e32 v140, v140, v142
	v_cndmask_b32_e64 v130, v128, v132, s[30:31]
	v_cndmask_b32_e64 v134, v136, v140, s[30:31]
	v_cndmask_b32_e64 v129, v132, v128, s[30:31]
	v_cndmask_b32_e64 v133, v140, v136, s[30:31]
	v_add_f32_dpp v129, v130, v129 quad_perm:[1,0,3,2] row_mask:0xf bank_mask:0xf bound_ctrl:1
	v_add_f32_dpp v133, v134, v133 quad_perm:[1,0,3,2] row_mask:0xf bank_mask:0xf bound_ctrl:1
	v_cndmask_b32_e64 v135, v129, v133, s[32:33]
	v_cndmask_b32_e64 v131, v133, v129, s[32:33]
	s_nop 1
	v_add_f32_dpp v131, v135, v131 quad_perm:[2,3,0,1] row_mask:0xf bank_mask:0xf bound_ctrl:1
	v_cvt_f16_f32_e32 v131, v131
	ds_write_b16 v14, v131 offset:0
	s_waitcnt vmcnt(24)
	v_add_f32_e32 v144, v144, v145
	v_add_f32_e32 v146, v146, v147
	v_add_f32_e32 v148, v148, v149
	v_add_f32_e32 v150, v150, v151
	v_add_f32_e32 v152, v152, v153
	v_add_f32_e32 v154, v154, v155
	v_add_f32_e32 v156, v156, v157
	v_add_f32_e32 v158, v158, v159
	v_add_f32_e32 v144, v144, v146
	v_add_f32_e32 v148, v148, v150
	v_add_f32_e32 v152, v152, v154
	v_add_f32_e32 v156, v156, v158
	v_cndmask_b32_e64 v146, v144, v148, s[30:31]
	v_cndmask_b32_e64 v150, v152, v156, s[30:31]
	v_cndmask_b32_e64 v145, v148, v144, s[30:31]
	v_cndmask_b32_e64 v149, v156, v152, s[30:31]
	v_add_f32_dpp v145, v146, v145 quad_perm:[1,0,3,2] row_mask:0xf bank_mask:0xf bound_ctrl:1
	v_add_f32_dpp v149, v150, v149 quad_perm:[1,0,3,2] row_mask:0xf bank_mask:0xf bound_ctrl:1
	v_cndmask_b32_e64 v151, v145, v149, s[32:33]
	v_cndmask_b32_e64 v147, v149, v145, s[32:33]
	s_nop 1
	v_add_f32_dpp v147, v151, v147 quad_perm:[2,3,0,1] row_mask:0xf bank_mask:0xf bound_ctrl:1
	v_cvt_f16_f32_e32 v147, v147
	ds_write_b16 v14, v147 offset:1088
	s_waitcnt vmcnt(20)
	v_add_f32_e32 v160, v160, v161
	v_add_f32_e32 v162, v162, v163
	v_add_f32_e32 v164, v164, v165
	v_add_f32_e32 v166, v166, v167
	v_add_f32_e32 v168, v168, v169
	v_add_f32_e32 v170, v170, v171
	v_add_f32_e32 v172, v172, v173
	v_add_f32_e32 v174, v174, v175
	v_add_f32_e32 v160, v160, v162
	v_add_f32_e32 v164, v164, v166
	v_add_f32_e32 v168, v168, v170
	v_add_f32_e32 v172, v172, v174
	v_cndmask_b32_e64 v162, v160, v164, s[30:31]
	v_cndmask_b32_e64 v166, v168, v172, s[30:31]
	v_cndmask_b32_e64 v161, v164, v160, s[30:31]
	v_cndmask_b32_e64 v165, v172, v168, s[30:31]
	v_add_f32_dpp v161, v162, v161 quad_perm:[1,0,3,2] row_mask:0xf bank_mask:0xf bound_ctrl:1
	v_add_f32_dpp v165, v166, v165 quad_perm:[1,0,3,2] row_mask:0xf bank_mask:0xf bound_ctrl:1
	v_cndmask_b32_e64 v167, v161, v165, s[32:33]
	v_cndmask_b32_e64 v163, v165, v161, s[32:33]
	s_nop 1
	v_add_f32_dpp v163, v167, v163 quad_perm:[2,3,0,1] row_mask:0xf bank_mask:0xf bound_ctrl:1
	v_cvt_f16_f32_e32 v163, v163
	ds_write_b16 v14, v163 offset:2176
	s_waitcnt vmcnt(16)
	v_add_f32_e32 v176, v176, v177
	v_add_f32_e32 v178, v178, v179
	v_add_f32_e32 v180, v180, v181
	v_add_f32_e32 v182, v182, v183
	v_add_f32_e32 v184, v184, v185
	v_add_f32_e32 v186, v186, v187
	v_add_f32_e32 v188, v188, v189
	v_add_f32_e32 v190, v190, v191
	v_add_f32_e32 v176, v176, v178
	v_add_f32_e32 v180, v180, v182
	v_add_f32_e32 v184, v184, v186
	v_add_f32_e32 v188, v188, v190
	v_cndmask_b32_e64 v178, v176, v180, s[30:31]
	v_cndmask_b32_e64 v182, v184, v188, s[30:31]
	v_cndmask_b32_e64 v177, v180, v176, s[30:31]
	v_cndmask_b32_e64 v181, v188, v184, s[30:31]
	v_add_f32_dpp v177, v178, v177 quad_perm:[1,0,3,2] row_mask:0xf bank_mask:0xf bound_ctrl:1
	v_add_f32_dpp v181, v182, v181 quad_perm:[1,0,3,2] row_mask:0xf bank_mask:0xf bound_ctrl:1
	v_cndmask_b32_e64 v183, v177, v181, s[32:33]
	v_cndmask_b32_e64 v179, v181, v177, s[32:33]
	s_nop 1
	v_add_f32_dpp v179, v183, v179 quad_perm:[2,3,0,1] row_mask:0xf bank_mask:0xf bound_ctrl:1
	v_cvt_f16_f32_e32 v179, v179
	ds_write_b16 v14, v179 offset:3264
	s_waitcnt vmcnt(12)
	v_add_f32_e32 v192, v192, v193
	v_add_f32_e32 v194, v194, v195
	v_add_f32_e32 v196, v196, v197
	v_add_f32_e32 v198, v198, v199
	v_add_f32_e32 v200, v200, v201
	v_add_f32_e32 v202, v202, v203
	v_add_f32_e32 v204, v204, v205
	v_add_f32_e32 v206, v206, v207
	v_add_f32_e32 v192, v192, v194
	v_add_f32_e32 v196, v196, v198
	v_add_f32_e32 v200, v200, v202
	v_add_f32_e32 v204, v204, v206
	v_cndmask_b32_e64 v194, v192, v196, s[30:31]
	v_cndmask_b32_e64 v198, v200, v204, s[30:31]
	v_cndmask_b32_e64 v193, v196, v192, s[30:31]
	v_cndmask_b32_e64 v197, v204, v200, s[30:31]
	v_add_f32_dpp v193, v194, v193 quad_perm:[1,0,3,2] row_mask:0xf bank_mask:0xf bound_ctrl:1
	v_add_f32_dpp v197, v198, v197 quad_perm:[1,0,3,2] row_mask:0xf bank_mask:0xf bound_ctrl:1
	v_cndmask_b32_e64 v199, v193, v197, s[32:33]
	v_cndmask_b32_e64 v195, v197, v193, s[32:33]
	s_nop 1
	v_add_f32_dpp v195, v199, v195 quad_perm:[2,3,0,1] row_mask:0xf bank_mask:0xf bound_ctrl:1
	v_cvt_f16_f32_e32 v195, v195
	ds_write_b16 v14, v195 offset:4352
	s_waitcnt vmcnt(8)
	v_add_f32_e32 v208, v208, v209
	v_add_f32_e32 v210, v210, v211
	v_add_f32_e32 v212, v212, v213
	v_add_f32_e32 v214, v214, v215
	v_add_f32_e32 v216, v216, v217
	v_add_f32_e32 v218, v218, v219
	v_add_f32_e32 v220, v220, v221
	v_add_f32_e32 v222, v222, v223
	v_add_f32_e32 v208, v208, v210
	v_add_f32_e32 v212, v212, v214
	v_add_f32_e32 v216, v216, v218
	v_add_f32_e32 v220, v220, v222
	v_cndmask_b32_e64 v210, v208, v212, s[30:31]
	v_cndmask_b32_e64 v214, v216, v220, s[30:31]
	v_cndmask_b32_e64 v209, v212, v208, s[30:31]
	v_cndmask_b32_e64 v213, v220, v216, s[30:31]
	v_add_f32_dpp v209, v210, v209 quad_perm:[1,0,3,2] row_mask:0xf bank_mask:0xf bound_ctrl:1
	v_add_f32_dpp v213, v214, v213 quad_perm:[1,0,3,2] row_mask:0xf bank_mask:0xf bound_ctrl:1
	v_cndmask_b32_e64 v215, v209, v213, s[32:33]
	v_cndmask_b32_e64 v211, v213, v209, s[32:33]
	s_nop 1
	v_add_f32_dpp v211, v215, v211 quad_perm:[2,3,0,1] row_mask:0xf bank_mask:0xf bound_ctrl:1
	v_cvt_f16_f32_e32 v211, v211
	ds_write_b16 v14, v211 offset:5440
	s_waitcnt vmcnt(4)
	v_add_f32_e32 v224, v224, v225
	v_add_f32_e32 v226, v226, v227
	v_add_f32_e32 v228, v228, v229
	v_add_f32_e32 v230, v230, v231
	v_add_f32_e32 v232, v232, v233
	v_add_f32_e32 v234, v234, v235
	v_add_f32_e32 v236, v236, v237
	v_add_f32_e32 v238, v238, v239
	v_add_f32_e32 v224, v224, v226
	v_add_f32_e32 v228, v228, v230
	v_add_f32_e32 v232, v232, v234
	v_add_f32_e32 v236, v236, v238
	v_cndmask_b32_e64 v226, v224, v228, s[30:31]
	v_cndmask_b32_e64 v230, v232, v236, s[30:31]
	v_cndmask_b32_e64 v225, v228, v224, s[30:31]
	v_cndmask_b32_e64 v229, v236, v232, s[30:31]
	v_add_f32_dpp v225, v226, v225 quad_perm:[1,0,3,2] row_mask:0xf bank_mask:0xf bound_ctrl:1
	v_add_f32_dpp v229, v230, v229 quad_perm:[1,0,3,2] row_mask:0xf bank_mask:0xf bound_ctrl:1
	v_cndmask_b32_e64 v231, v225, v229, s[32:33]
	v_cndmask_b32_e64 v227, v229, v225, s[32:33]
	s_nop 1
	v_add_f32_dpp v227, v231, v227 quad_perm:[2,3,0,1] row_mask:0xf bank_mask:0xf bound_ctrl:1
	v_cvt_f16_f32_e32 v227, v227
	ds_write_b16 v14, v227 offset:6528
	s_waitcnt vmcnt(0)
	v_add_f32_e32 v240, v240, v241
	v_add_f32_e32 v242, v242, v243
	v_add_f32_e32 v244, v244, v245
	v_add_f32_e32 v246, v246, v247
	v_add_f32_e32 v248, v248, v249
	v_add_f32_e32 v250, v250, v251
	v_add_f32_e32 v252, v252, v253
	v_add_f32_e32 v254, v254, v255
	v_add_f32_e32 v240, v240, v242
	v_add_f32_e32 v244, v244, v246
	v_add_f32_e32 v248, v248, v250
	v_add_f32_e32 v252, v252, v254
	v_cndmask_b32_e64 v242, v240, v244, s[30:31]
	v_cndmask_b32_e64 v246, v248, v252, s[30:31]
	v_cndmask_b32_e64 v241, v244, v240, s[30:31]
	v_cndmask_b32_e64 v245, v252, v248, s[30:31]
	v_add_f32_dpp v241, v242, v241 quad_perm:[1,0,3,2] row_mask:0xf bank_mask:0xf bound_ctrl:1
	v_add_f32_dpp v245, v246, v245 quad_perm:[1,0,3,2] row_mask:0xf bank_mask:0xf bound_ctrl:1
	v_cndmask_b32_e64 v247, v241, v245, s[32:33]
	v_cndmask_b32_e64 v243, v245, v241, s[32:33]
	s_nop 1
	v_add_f32_dpp v243, v247, v243 quad_perm:[2,3,0,1] row_mask:0xf bank_mask:0xf bound_ctrl:1
	v_cvt_f16_f32_e32 v243, v243
	ds_write_b16 v14, v243 offset:7616
	s_waitcnt lgkmcnt(0)
	s_barrier
	ds_read_b128 v[160:163], v15 offset:0
	ds_read_b128 v[164:167], v15 offset:32
	ds_read_b128 v[168:171], v15 offset:64
	ds_read_b128 v[172:175], v15 offset:96
	ds_read_b128 v[176:179], v15 offset:128
	ds_read_b128 v[180:183], v15 offset:160
	ds_read_b128 v[184:187], v15 offset:192
	ds_read_b128 v[188:191], v15 offset:224
	s_waitcnt lgkmcnt(7)
	v_mfma_f32_32x32x16_f16 v[128:143], v[160:163], v[32:35], 0
	v_mfma_f32_32x32x16_f16 v[144:159], v[160:163], v[64:67], 0
	s_waitcnt lgkmcnt(6)
	v_mfma_f32_32x32x16_f16 v[128:143], v[164:167], v[36:39], v[128:143]
	v_mfma_f32_32x32x16_f16 v[144:159], v[164:167], v[68:71], v[144:159]
	s_waitcnt lgkmcnt(5)
	v_mfma_f32_32x32x16_f16 v[128:143], v[168:171], v[40:43], v[128:143]
	v_mfma_f32_32x32x16_f16 v[144:159], v[168:171], v[72:75], v[144:159]
	s_waitcnt lgkmcnt(4)
	v_mfma_f32_32x32x16_f16 v[128:143], v[172:175], v[44:47], v[128:143]
	v_mfma_f32_32x32x16_f16 v[144:159], v[172:175], v[76:79], v[144:159]
	s_waitcnt lgkmcnt(3)
	v_mfma_f32_32x32x16_f16 v[128:143], v[176:179], v[48:51], v[128:143]
	v_mfma_f32_32x32x16_f16 v[144:159], v[176:179], v[80:83], v[144:159]
	s_waitcnt lgkmcnt(2)
	v_mfma_f32_32x32x16_f16 v[128:143], v[180:183], v[52:55], v[128:143]
	v_mfma_f32_32x32x16_f16 v[144:159], v[180:183], v[84:87], v[144:159]
	s_waitcnt lgkmcnt(1)
	v_mfma_f32_32x32x16_f16 v[128:143], v[184:187], v[56:59], v[128:143]
	v_mfma_f32_32x32x16_f16 v[144:159], v[184:187], v[88:91], v[144:159]
	s_waitcnt lgkmcnt(0)
	v_mfma_f32_32x32x16_f16 v[128:143], v[188:191], v[60:63], v[128:143]
	v_mfma_f32_32x32x16_f16 v[144:159], v[188:191], v[92:95], v[144:159]
	s_nop 15
	s_nop 3
	v_mul_f32_e32 v16, v96, v128
	v_mul_f32_e32 v17, v97, v129
	v_mul_f32_e32 v18, v98, v130
	v_mul_f32_e32 v19, v99, v131
	v_fma_f32 v16, -v112, v144, v16
	v_fma_f32 v17, -v113, v145, v17
	v_fma_f32 v18, -v114, v146, v18
	v_fma_f32 v19, -v115, v147, v19
	v_fma_f32 v16, v100, v132, v16
	v_fma_f32 v16, -v116, v148, v16
	v_fma_f32 v17, v101, v133, v17
	v_fma_f32 v17, -v117, v149, v17
	v_fma_f32 v18, v102, v134, v18
	v_fma_f32 v18, -v118, v150, v18
	v_fma_f32 v19, v103, v135, v19
	v_fma_f32 v19, -v119, v151, v19
	v_fma_f32 v16, v104, v136, v16
	v_fma_f32 v16, -v120, v152, v16
	v_fma_f32 v17, v105, v137, v17
	v_fma_f32 v17, -v121, v153, v17
	v_fma_f32 v18, v106, v138, v18
	v_fma_f32 v18, -v122, v154, v18
	v_fma_f32 v19, v107, v139, v19
	v_fma_f32 v19, -v123, v155, v19
	v_fma_f32 v16, v108, v140, v16
	v_fma_f32 v16, -v124, v156, v16
	v_fma_f32 v17, v109, v141, v17
	v_fma_f32 v17, -v125, v157, v17
	v_fma_f32 v18, v110, v142, v18
	v_fma_f32 v18, -v126, v158, v18
	v_fma_f32 v19, v111, v143, v19
	v_fma_f32 v19, -v127, v159, v19
	v_add_f32_e32 v16, v16, v17
	v_add_f32_e32 v18, v18, v19
	v_add_f32_e32 v16, v16, v18
	v_mov_b32_e32 v17, v16
	s_lshl_b32 s6, s6, 6
	s_add_i32 s6, s6, s7
	s_lshl_b32 s6, s6, 10
	v_permlane32_swap_b32_e32 v16, v17
	v_add_u32_e32 v5, s6, v5
	v_cmp_gt_u32_e32 vcc, 32, v1
	v_add_f32_e32 v16, v16, v17
	s_and_saveexec_b64 s[2:3], vcc
	s_cbranch_execz .Ldog_main_done
	global_store_dword v5, v16, s[26:27]

_Z7dog_finPKfS0_Pf:
	s_load_dwordx4 s[4:7], s[0:1], 0x0
	s_load_dwordx2 s[8:9], s[0:1], 0x10
	s_and_b32 s3, s2, 7
	s_lshl_b32 s3, s3, 3
	s_lshr_b32 s10, s2, 3
	s_add_i32 s3, s3, s10
	v_lshlrev_b32_e32 v1, 2, v0
	s_lshl_b32 s3, s3, 10
	v_add_u32_e32 v2, s3, v1
	v_add_u32_e32 v3, 0x10000, v2
	v_add_u32_e32 v4, 0x20000, v2
	v_add_u32_e32 v5, 0x30000, v2
	s_waitcnt lgkmcnt(0)
	global_load_dword v12, v2, s[4:5]
	global_load_dword v14, v3, s[4:5]
	global_load_dword v13, v4, s[4:5]
	global_load_dword v15, v5, s[4:5]
	global_load_dword v6, v1, s[6:7]
	global_load_dword v7, v2, s[8:9]
	s_waitcnt vmcnt(2)
	v_pk_add_f32 v[8:9], v[12:13], v[14:15]
	s_nop 0
	v_add_f32_e32 v8, v8, v9
	s_waitcnt vmcnt(1)
	v_add_f32_e32 v6, v6, v8
	global_store_dword v2, v6, s[8:9]
	s_endpgm

	.amdhsa_kernel _Z7dog_finPKfS0_Pf
		.amdhsa_group_segment_fixed_size 0
		.amdhsa_private_segment_fixed_size 0
		.amdhsa_kernarg_size 24
		.amdhsa_user_sgpr_count 2
		.amdhsa_user_sgpr_dispatch_ptr 0
		.amdhsa_user_sgpr_queue_ptr 0
		.amdhsa_user_sgpr_kernarg_segment_ptr 1
		.amdhsa_user_sgpr_dispatch_id 0
		.amdhsa_user_sgpr_kernarg_preload_length 0
		.amdhsa_user_sgpr_kernarg_preload_offset 0
		.amdhsa_user_sgpr_private_segment_size 0
		.amdhsa_uses_dynamic_stack 0
		.amdhsa_enable_private_segment 0
		.amdhsa_system_sgpr_workgroup_id_x 1
		.amdhsa_system_sgpr_workgroup_id_y 0
		.amdhsa_system_sgpr_workgroup_id_z 0
		.amdhsa_system_sgpr_workgroup_info 0
		.amdhsa_system_vgpr_workitem_id 0
		.amdhsa_next_free_vgpr 16
		.amdhsa_next_free_sgpr 16
		.amdhsa_accum_offset 16
		.amdhsa_reserve_vcc 1
		.amdhsa_float_round_mode_32 0
		.amdhsa_float_round_mode_16_64 0
		.amdhsa_float_denorm_mode_32 3
		.amdhsa_float_denorm_mode_16_64 3
		.amdhsa_dx10_clamp 1
		.amdhsa_ieee_mode 1
		.amdhsa_fp16_overflow 0
		.amdhsa_tg_split 0
		.amdhsa_exception_fp_ieee_invalid_op 0
		.amdhsa_exception_fp_denorm_src 0
		.amdhsa_exception_fp_ieee_div_zero 0
		.amdhsa_exception_fp_ieee_overflow 0
		.amdhsa_exception_fp_ieee_underflow 0
		.amdhsa_exception_fp_ieee_inexact 0
		.amdhsa_exception_int_div_zero 0
	.end_amdhsa_kernel

.Lfunc_end1:
	.size	_Z7dog_finPKfS0_Pf, .Lfunc_end1-_Z7dog_finPKfS0_Pf
	.set _Z7dog_finPKfS0_Pf.num_vgpr, 16
	.set _Z7dog_finPKfS0_Pf.num_agpr, 0
	.set _Z7dog_finPKfS0_Pf.numbered_sgpr, 11
	.set _Z7dog_finPKfS0_Pf.num_named_barrier, 0
	.set _Z7dog_finPKfS0_Pf.private_seg_size, 0
	.set _Z7dog_finPKfS0_Pf.uses_vcc, 1
	.set _Z7dog_finPKfS0_Pf.uses_flat_scratch, 0
	.set _Z7dog_finPKfS0_Pf.has_dyn_sized_stack, 0
	.set _Z7dog_finPKfS0_Pf.has_recursion, 0
	.set _Z7dog_finPKfS0_Pf.has_indirect_call, 0
